# variant A plus 128-byte alignment of the attention main-loop back-edge block (both layers)
# speedup vs baseline: 1.0038x; 1.0026x over previous
.LBB0_1612:
	v_sub_f32_e32 v64, v64, v65
	v_mov_b32_e32 v65, v64
	v_mov_b32_e32 v66, v64
	v_mov_b32_e32 v67, v64
	v_mov_b32_e32 v68, v64
	v_mov_b32_e32 v69, v64
	v_mov_b32_e32 v70, v64
	v_mov_b32_e32 v71, v64
	v_mov_b32_e32 v72, v64
	v_mov_b32_e32 v73, v64
	v_mov_b32_e32 v74, v64
	v_mov_b32_e32 v75, v64
	v_mov_b32_e32 v76, v64
	v_mov_b32_e32 v77, v64
	v_mov_b32_e32 v78, v64
	v_mov_b32_e32 v79, v64
	v_mul_u32_u24_e32 v80, 0x50, v194
	v_add3_u32 v198, 0, v184, v80
	s_mov_b32 s16, 2
	s_mov_b32 s18, 0
	s_mov_b32 s17, 1
	s_movk_i32 s19, 0x4000
	s_mov_b32 s20, 0xc000
	s_mov_b32 s13, 0
	s_branch .LBB0_1614
	.p2align 7
